# speedup vs baseline: 1.0040x; 1.0040x over previous
_Z9fast_mainILb0EEvPKiS1_S1_PKfPKcS3_PfS6_PiPyS6_:
	s_nop 0
	s_nop 0
	s_load_dwordx4 s[4:7], s[0:1], 0x20
	s_load_dwordx4 s[8:11], s[0:1], 0x8
	s_load_dwordx2 s[16:17], s[0:1], 0x0
	v_and_b32_e32 v1, 63, v0
	v_lshrrev_b32_e32 v8, 6, v0
	v_lshlrev_b32_e32 v150, 4, v1
	v_lshl_or_b32 v14, s2, 3, v8
	v_lshlrev_b32_e32 v14, 10, v14
	v_or_b32_e32 v14, v14, v150
	v_add_u32_e32 v212, 0x10000, v150
	v_add_u32_e32 v213, 0x18c00, v150
	v_mov_b32_e32 v151, 0
	s_waitcnt lgkmcnt(0)
	global_load_dwordx4 v[20:23], v14, s[16:17]
	v_lshl_add_u64 v[4:5], s[4:5], 0, v[150:151]
	v_lshlrev_b32_e32 v2, 10, v8
	v_mov_b32_e32 v3, v151
	v_lshl_add_u64 v[6:7], v[4:5], 0, v[2:3]
	v_readfirstlane_b32 s3, v2
	v_or_b32_e32 v3, 0x2000, v2
	s_mov_b32 m0, s3
	s_mov_b64 s[4:5], 0x2000
	v_readfirstlane_b32 s3, v3
	global_load_lds_dwordx4 v[6:7], off
	v_lshl_add_u64 v[10:11], v[6:7], 0, s[4:5]
	s_mov_b32 m0, s3
	v_or_b32_e32 v3, 0x6000, v2
	global_load_lds_dwordx4 v[10:11], off
	v_or_b32_e32 v10, 0x4000, v2
	v_mov_b32_e32 v11, v151
	v_readfirstlane_b32 s3, v10
	v_lshl_add_u64 v[12:13], v[4:5], 0, v[10:11]
	s_mov_b32 m0, s3
	s_mov_b64 s[4:5], 0x6000
	v_readfirstlane_b32 s3, v3
	global_load_lds_dwordx4 v[12:13], off
	v_lshl_add_u64 v[10:11], v[6:7], 0, s[4:5]
	s_mov_b32 m0, s3
	v_or_b32_e32 v3, 0xa000, v2
	global_load_lds_dwordx4 v[10:11], off
	v_or_b32_e32 v10, 0x8000, v2
	v_mov_b32_e32 v11, v151
	v_readfirstlane_b32 s3, v10
	v_lshl_add_u64 v[12:13], v[4:5], 0, v[10:11]
	s_mov_b32 m0, s3
	s_mov_b64 s[4:5], 0xa000
	v_readfirstlane_b32 s3, v3
	global_load_lds_dwordx4 v[12:13], off
	v_lshl_add_u64 v[10:11], v[6:7], 0, s[4:5]
	s_mov_b32 m0, s3
	v_or_b32_e32 v3, 0xe000, v2
	global_load_lds_dwordx4 v[10:11], off
	v_or_b32_e32 v10, 0xc000, v2
	v_mov_b32_e32 v11, v151
	v_readfirstlane_b32 s3, v10
	v_lshl_add_u64 v[12:13], v[4:5], 0, v[10:11]
	s_mov_b32 m0, s3
	s_mov_b64 s[4:5], 0xe000
	v_readfirstlane_b32 s3, v3
	global_load_lds_dwordx4 v[12:13], off
	v_lshl_add_u64 v[10:11], v[6:7], 0, s[4:5]
	s_mov_b32 m0, s3
	v_or_b32_e32 v3, 0x12000, v2
	global_load_lds_dwordx4 v[10:11], off
	v_or_b32_e32 v10, 0x10000, v2
	v_mov_b32_e32 v11, v151
	v_readfirstlane_b32 s3, v10
	v_lshl_add_u64 v[12:13], v[4:5], 0, v[10:11]
	s_mov_b32 m0, s3
	s_mov_b64 s[4:5], 0x12000
	v_readfirstlane_b32 s3, v3
	global_load_lds_dwordx4 v[12:13], off
	v_lshl_add_u64 v[10:11], v[6:7], 0, s[4:5]
	s_mov_b32 m0, s3
	s_nop 0
	global_load_lds_dwordx4 v[10:11], off
	v_or_b32_e32 v10, 0x14000, v2
	v_mov_b32_e32 v11, v151
	v_readfirstlane_b32 s3, v10
	v_lshl_add_u64 v[12:13], v[4:5], 0, v[10:11]
	s_mov_b32 m0, s3
	s_movk_i32 s3, 0x2c0
	global_load_lds_dwordx4 v[12:13], off
	v_cmp_gt_u32_e32 vcc, s3, v0
	s_and_saveexec_b64 s[4:5], vcc
	s_cbranch_execz .LBB1_2
	v_or_b32_e32 v3, 0x16000, v2
	s_mov_b64 s[12:13], 0x16000
	v_readfirstlane_b32 s3, v3
	v_lshl_add_u64 v[6:7], v[6:7], 0, s[12:13]
	s_mov_b32 m0, s3
	s_nop 0
	global_load_lds_dwordx4 v[6:7], off
